# norm phases (mix L1, ffn, router): all latent rows of a wave prefetched up front into register banks, counted waits instead of one exposed round trip per row
# baseline (speedup 1.0000x reference)
; template <bool ROUTER, bool SMALLP>
; __device__ __forceinline__ void norm_phase(KA A, LAS unsigned char* lds, int l, int which, int npart, const float* pgate, int tid, int wave, int lane, int bid) {
;     ...
;     f32x4 vnx[8]; v4u vnb[4]; bool nb;
;     NORM_LOAD(wave);
.LBB0_610:
	s_mov_b32 s101, 0
	s_and_b64 vcc, exec, s[12:13]
	v_lshlrev_b32_e32 v50, 4, v222
	s_cbranch_vccz .LBB0_612
	s_ashr_i32 s11, s10, 31
	s_lshl_b64 s[10:11], s[10:11], 12
	s_add_u32 s10, s6, s10
	s_addc_u32 s11, s7, s11
	global_load_dwordx4 v[34:37], v50, s[10:11]
	global_load_dwordx4 v[38:41], v50, s[10:11] offset:1024
	global_load_dwordx4 v[42:45], v50, s[10:11] offset:2048
	global_load_dwordx4 v[46:49], v50, s[10:11] offset:3072
	s_mov_b32 s101, 1
	s_add_u32 s10, s10, 0x8000
	s_addc_u32 s11, s11, 0
	global_load_dwordx4 v[134:137], v50, s[10:11]
	global_load_dwordx4 v[138:141], v50, s[10:11] offset:1024
	global_load_dwordx4 v[142:145], v50, s[10:11] offset:2048
	global_load_dwordx4 v[146:149], v50, s[10:11] offset:3072
	s_add_u32 s10, s10, 0x8000
	s_addc_u32 s11, s11, 0
	global_load_dwordx4 v[150:153], v50, s[10:11]
	global_load_dwordx4 v[154:157], v50, s[10:11] offset:1024
	global_load_dwordx4 v[158:161], v50, s[10:11] offset:2048
	global_load_dwordx4 v[162:165], v50, s[10:11] offset:3072
	s_add_u32 s10, s10, 0x8000
	s_addc_u32 s11, s11, 0
	global_load_dwordx4 v[166:169], v50, s[10:11]
	global_load_dwordx4 v[170:173], v50, s[10:11] offset:1024
	global_load_dwordx4 v[174:177], v50, s[10:11] offset:2048
	global_load_dwordx4 v[178:181], v50, s[10:11] offset:3072

; __device__ __forceinline__ int wg_row(int bid, int rl) { if (rl < 32) return (bid >> 7) * TB + CTXL + 32 * (bid & 127) + rl; const int q = 2 * bid + (rl - 32); return (q >> 8) * TB + (q & 255); }
; template <bool ROUTER, bool SMALLP>
; __device__ __forceinline__ void norm_phase(KA A, LAS unsigned char* lds, int l, int which, int npart, const float* pgate, int tid, int wave, int lane, int bid) {
;     ...
;     for (int rl = wave; rl < 34; rl += NWAVES) {
;         const int row = wg_row(bid, rl), s = row % TB; const bool isctx = s < CTXL; const int b = row / TB;
;         f32x4 v[8]; float ss = 0.f;
;         if (nb) {
; #pragma unroll
;             for (int jj = 0; jj < 4; ++jj) { float f[8]; unpack8(vnb[jj], f); v[2 * jj] = (f32x4){f[0], f[1], f[2], f[3]}; v[2 * jj + 1] = (f32x4){f[4], f[5], f[6], f[7]}; }
;         } else {
; #pragma unroll
;             for (int j = 0; j < 8; ++j) v[j] = vnx[j];
;         }
.LBB0_622:
	s_cmp_lt_i32 s27, 32
	s_cselect_b32 vcc_lo, s101, 0
	s_cmp_lg_u32 vcc_lo, 0
	s_cbranch_scc0 .Lnbk_otop_A
	s_waitcnt vmcnt(12)
	s_branch .Lnbk_unpack_A

; __device__ __forceinline__ void unpack8(const v4u v, float (&f)[8]) {
;     f[0] = __uint_as_float(v.x << 16); f[1] = __uint_as_float(v.x & 0xffff0000u); f[2] = __uint_as_float(v.y << 16); f[3] = __uint_as_float(v.y & 0xffff0000u);
;     f[4] = __uint_as_float(v.z << 16); f[5] = __uint_as_float(v.z & 0xffff0000u); f[6] = __uint_as_float(v.w << 16); f[7] = __uint_as_float(v.w & 0xffff0000u); }
; template <bool ROUTER, bool SMALLP>
; __device__ __forceinline__ void norm_phase(KA A, LAS unsigned char* lds, int l, int which, int npart, const float* pgate, int tid, int wave, int lane, int bid) {
;     ...
;         if (nb) {
; #pragma unroll
;             for (int jj = 0; jj < 4; ++jj) { float f[8]; unpack8(vnb[jj], f); v[2 * jj] = (f32x4){f[0], f[1], f[2], f[3]}; v[2 * jj + 1] = (f32x4){f[4], f[5], f[6], f[7]}; }
;         } else {
; #pragma unroll
;             for (int j = 0; j < 8; ++j) v[j] = vnx[j];
;         }
;         if (rl + NWAVES < 34) NORM_LOAD(rl + NWAVES);
.Lnbk_unpack_A:
	v_lshlrev_b32_e32 v78, 16, v34
	v_and_b32_e32 v79, 0xffff0000, v34
	v_lshlrev_b32_e32 v80, 16, v35
	v_and_b32_e32 v81, 0xffff0000, v35
	v_lshlrev_b32_e32 v70, 16, v36
	v_and_b32_e32 v71, 0xffff0000, v36
	v_lshlrev_b32_e32 v72, 16, v37
	v_and_b32_e32 v73, 0xffff0000, v37
	v_lshlrev_b32_e32 v74, 16, v38
	v_and_b32_e32 v75, 0xffff0000, v38
	v_lshlrev_b32_e32 v76, 16, v39
	v_and_b32_e32 v77, 0xffff0000, v39
	v_lshlrev_b32_e32 v62, 16, v40
	v_and_b32_e32 v63, 0xffff0000, v40
	v_lshlrev_b32_e32 v64, 16, v41
	v_and_b32_e32 v65, 0xffff0000, v41
	v_lshlrev_b32_e32 v66, 16, v42
	v_and_b32_e32 v67, 0xffff0000, v42
	v_lshlrev_b32_e32 v68, 16, v43
	v_and_b32_e32 v69, 0xffff0000, v43
	v_lshlrev_b32_e32 v54, 16, v44
	v_and_b32_e32 v55, 0xffff0000, v44
	v_lshlrev_b32_e32 v56, 16, v45
	v_and_b32_e32 v57, 0xffff0000, v45
	v_lshlrev_b32_e32 v58, 16, v46
	v_and_b32_e32 v59, 0xffff0000, v46
	v_lshlrev_b32_e32 v60, 16, v47
	v_and_b32_e32 v61, 0xffff0000, v47
	v_lshlrev_b32_e32 v50, 16, v48
	v_and_b32_e32 v51, 0xffff0000, v48
	v_lshlrev_b32_e32 v52, 16, v49
	v_and_b32_e32 v53, 0xffff0000, v49
.LBB0_624:
	s_cmp_gt_i32 s27, 25
	s_cselect_b64 s[22:23], -1, 0
	s_and_b64 vcc, exec, s[22:23]
	s_cbranch_vccnz .LBB0_638
	s_cmp_lt_i32 s27, 24
	s_cselect_b32 vcc_lo, s101, 0
	s_cmp_lg_u32 vcc_lo, 0
	s_cbranch_scc0 .Lnbk_omid_A
	s_waitcnt vmcnt(8)
	s_cmp_gt_i32 s27, 7
	s_cbranch_scc1 .Lnbk_b2_A
	v_mov_b64_e32 v[34:35], v[134:135]
	v_mov_b64_e32 v[36:37], v[136:137]
	v_mov_b64_e32 v[38:39], v[138:139]
	v_mov_b64_e32 v[40:41], v[140:141]
	v_mov_b64_e32 v[42:43], v[142:143]
	v_mov_b64_e32 v[44:45], v[144:145]
	v_mov_b64_e32 v[46:47], v[146:147]
	v_mov_b64_e32 v[48:49], v[148:149]
	s_branch .LBB0_638
.Lnbk_b2_A:
	s_cmp_gt_i32 s27, 15
	s_cbranch_scc1 .Lnbk_b3_A
	v_mov_b64_e32 v[34:35], v[150:151]
	v_mov_b64_e32 v[36:37], v[152:153]
	v_mov_b64_e32 v[38:39], v[154:155]
	v_mov_b64_e32 v[40:41], v[156:157]
	v_mov_b64_e32 v[42:43], v[158:159]
	v_mov_b64_e32 v[44:45], v[160:161]
	v_mov_b64_e32 v[46:47], v[162:163]
	v_mov_b64_e32 v[48:49], v[164:165]
	s_branch .LBB0_638
.Lnbk_b3_A:
	v_mov_b64_e32 v[34:35], v[166:167]
	v_mov_b64_e32 v[36:37], v[168:169]
	v_mov_b64_e32 v[38:39], v[170:171]
	v_mov_b64_e32 v[40:41], v[172:173]
	v_mov_b64_e32 v[42:43], v[174:175]
	v_mov_b64_e32 v[44:45], v[176:177]
	v_mov_b64_e32 v[46:47], v[178:179]
	v_mov_b64_e32 v[48:49], v[180:181]
	s_branch .LBB0_638
.Lnbk_omid_A:
	s_cmp_gt_i32 s27, 23
	s_mov_b64 s[12:13], -1
	s_cbranch_scc0 .LBB0_627
	s_add_i32 s6, s19, s27
	s_lshr_b32 s7, s6, 8
	s_mulk_i32 s7, 0x1100
	s_and_b32 s6, s6, 0xff
	s_or_b32 s6, s7, s6
	s_cbranch_execnz .LBB0_629
	s_branch .LBB0_628

; template <bool ROUTER, bool SMALLP>
; __device__ __forceinline__ void norm_phase(KA A, LAS unsigned char* lds, int l, int which, int npart, const float* pgate, int tid, int wave, int lane, int bid) {
;     ...
;     f32x4 vnx[8]; v4u vnb[4]; bool nb;
;     NORM_LOAD(wave);
.LBB0_1692:
	s_add_u32 s6, s0, 0x33000000
	s_addc_u32 s7, s1, 0
	s_ashr_i32 s5, s4, 31
	s_lshl_b64 s[4:5], s[4:5], 12
	v_and_b32_e32 v4, 63, v34
	s_add_u32 s4, s6, s4
	v_lshlrev_b32_e32 v2, 4, v4
	s_addc_u32 s5, s7, s5
	global_load_dwordx4 v[18:21], v2, s[4:5] offset:3072
	global_load_dwordx4 v[22:25], v2, s[4:5] offset:2048
	global_load_dwordx4 v[26:29], v2, s[4:5] offset:1024
	global_load_dwordx4 v[30:33], v2, s[4:5]
	s_add_u32 s4, s4, 0x8000
	s_addc_u32 s5, s5, 0
	global_load_dwordx4 v[78:81], v2, s[4:5] offset:3072
	global_load_dwordx4 v[82:85], v2, s[4:5] offset:2048
	global_load_dwordx4 v[86:89], v2, s[4:5] offset:1024
	global_load_dwordx4 v[90:93], v2, s[4:5]
	s_add_u32 s4, s4, 0x8000
	s_addc_u32 s5, s5, 0
	global_load_dwordx4 v[94:97], v2, s[4:5] offset:3072
	global_load_dwordx4 v[98:101], v2, s[4:5] offset:2048
	global_load_dwordx4 v[102:105], v2, s[4:5] offset:1024
	global_load_dwordx4 v[106:109], v2, s[4:5]
	s_add_u32 s4, s4, 0x8000
	s_addc_u32 s5, s5, 0
	global_load_dwordx4 v[110:113], v2, s[4:5] offset:3072
	global_load_dwordx4 v[114:117], v2, s[4:5] offset:2048
	global_load_dwordx4 v[118:121], v2, s[4:5] offset:1024
	global_load_dwordx4 v[122:125], v2, s[4:5]
	s_lshl_b32 s2, s12, 5
	v_mov_b32_e32 v3, v130
	s_mul_i32 s16, s13, 0x1100
	s_and_b32 s2, s2, 0xfe0
	v_lshl_add_u64 v[36:37], s[6:7], 0, v[2:3]
	v_lshlrev_b32_e32 v2, 3, v4
	s_add_i32 s16, s16, s2
	s_lshl_b32 s2, s14, 4
	v_lshl_add_u64 v[2:3], s[0:1], 0, v[2:3]
	s_mov_b64 s[4:5], 0x37400000
	v_lshl_add_u32 v35, v4, 5, 0
	s_add_i32 s2, s2, 0
	v_lshl_add_u64 v[38:39], v[2:3], 0, s[4:5]
	s_lshl_b32 s15, s12, 1
	v_add_u32_e32 v58, 0x8000, v35
	v_cmp_eq_u32_e64 s[38:39], 0, v4
	s_add_i32 s17, s2, 0x1800c
	s_branch .LBB0_1694

; template <bool ROUTER, bool SMALLP>
; __device__ __forceinline__ void norm_phase(KA A, LAS unsigned char* lds, int l, int which, int npart, const float* pgate, int tid, int wave, int lane, int bid) {
;     ...
;         if (nb) {
; #pragma unroll
;             for (int jj = 0; jj < 4; ++jj) { float f[8]; unpack8(vnb[jj], f); v[2 * jj] = (f32x4){f[0], f[1], f[2], f[3]}; v[2 * jj + 1] = (f32x4){f[4], f[5], f[6], f[7]}; }
;         } else {
; #pragma unroll
;             for (int j = 0; j < 8; ++j) v[j] = vnx[j];
;         }
;         if (rl + NWAVES < 34) NORM_LOAD(rl + NWAVES);
.LBB0_1698:
	s_cmp_gt_i32 s14, 25
	s_cselect_b64 s[8:9], -1, 0
	s_waitcnt vmcnt(12)
	v_mov_b64_e32 v[2:3], v[18:19]
	v_mov_b64_e32 v[6:7], v[22:23]
	v_mov_b64_e32 v[10:11], v[26:27]
	v_mov_b64_e32 v[14:15], v[30:31]
	s_and_b64 vcc, exec, s[8:9]
	v_mov_b64_e32 v[4:5], v[20:21]
	v_mov_b64_e32 v[8:9], v[24:25]
	v_mov_b64_e32 v[12:13], v[28:29]
	v_mov_b64_e32 v[16:17], v[32:33]
	s_cbranch_vccnz .LBB0_1704
	s_cmp_lt_i32 s14, 24
	s_cbranch_scc0 .Lnbk_omid_C
	s_waitcnt vmcnt(8)
	s_cmp_gt_i32 s14, 7
	s_cbranch_scc1 .Lnbk_b2_C
	v_mov_b64_e32 v[2:3], v[78:79]
	v_mov_b64_e32 v[4:5], v[80:81]
	v_mov_b64_e32 v[6:7], v[82:83]
	v_mov_b64_e32 v[8:9], v[84:85]
	v_mov_b64_e32 v[10:11], v[86:87]
	v_mov_b64_e32 v[12:13], v[88:89]
	v_mov_b64_e32 v[14:15], v[90:91]
	v_mov_b64_e32 v[16:17], v[92:93]
	s_branch .LBB0_1704
.Lnbk_b2_C:
	s_cmp_gt_i32 s14, 15
	s_cbranch_scc1 .Lnbk_b3_C
	v_mov_b64_e32 v[2:3], v[94:95]
	v_mov_b64_e32 v[4:5], v[96:97]
	v_mov_b64_e32 v[6:7], v[98:99]
	v_mov_b64_e32 v[8:9], v[100:101]
	v_mov_b64_e32 v[10:11], v[102:103]
	v_mov_b64_e32 v[12:13], v[104:105]
	v_mov_b64_e32 v[14:15], v[106:107]
	v_mov_b64_e32 v[16:17], v[108:109]
	s_branch .LBB0_1704
.Lnbk_b3_C:
	v_mov_b64_e32 v[2:3], v[110:111]
	v_mov_b64_e32 v[4:5], v[112:113]
	v_mov_b64_e32 v[6:7], v[114:115]
	v_mov_b64_e32 v[8:9], v[116:117]
	v_mov_b64_e32 v[10:11], v[118:119]
	v_mov_b64_e32 v[12:13], v[120:121]
	v_mov_b64_e32 v[14:15], v[122:123]
	v_mov_b64_e32 v[16:17], v[124:125]
	s_branch .LBB0_1704
.Lnbk_omid_C:
	s_cmp_gt_i32 s14, 23
	s_mov_b64 s[10:11], -1
	s_cbranch_scc0 .LBB0_1701
	s_add_i32 s2, s15, s14
	s_sub_i32 s2, s2, 24
	s_lshr_b32 s5, s2, 8
	s_mulk_i32 s5, 0x1100
	s_and_b32 s2, s2, 0xff
	s_or_b32 s6, s5, s2
	s_mov_b64 s[10:11], 0

; template <bool ROUTER, bool SMALLP>
; __device__ __forceinline__ void norm_phase(KA A, LAS unsigned char* lds, int l, int which, int npart, const float* pgate, int tid, int wave, int lane, int bid) {
;     ...
;     f32x4 vnx[8]; v4u vnb[4]; bool nb;
;     NORM_LOAD(wave);
.LBB0_2191:
	s_mov_b32 s101, 0
	s_andn2_b64 vcc, exec, s[12:13]
	v_lshlrev_b32_e32 v52, 4, v53
	s_cbranch_vccnz .LBB0_2193
	s_ashr_i32 s11, s10, 31
	s_lshl_b64 s[10:11], s[10:11], 12
	s_add_u32 s10, s8, s10
	s_addc_u32 s11, s9, s11
	global_load_dwordx4 v[34:37], v52, s[10:11]
	global_load_dwordx4 v[38:41], v52, s[10:11] offset:1024
	global_load_dwordx4 v[42:45], v52, s[10:11] offset:2048
	global_load_dwordx4 v[46:49], v52, s[10:11] offset:3072
	s_mov_b32 s101, 1
	s_add_u32 s10, s10, 0x8000
	s_addc_u32 s11, s11, 0
	global_load_dwordx4 v[134:137], v52, s[10:11]
	global_load_dwordx4 v[138:141], v52, s[10:11] offset:1024
	global_load_dwordx4 v[142:145], v52, s[10:11] offset:2048
	global_load_dwordx4 v[146:149], v52, s[10:11] offset:3072
	s_add_u32 s10, s10, 0x8000
	s_addc_u32 s11, s11, 0
	global_load_dwordx4 v[150:153], v52, s[10:11]
	global_load_dwordx4 v[154:157], v52, s[10:11] offset:1024
	global_load_dwordx4 v[158:161], v52, s[10:11] offset:2048
	global_load_dwordx4 v[162:165], v52, s[10:11] offset:3072
	s_add_u32 s10, s10, 0x8000
	s_addc_u32 s11, s11, 0
	global_load_dwordx4 v[166:169], v52, s[10:11]
	global_load_dwordx4 v[170:173], v52, s[10:11] offset:1024
	global_load_dwordx4 v[174:177], v52, s[10:11] offset:2048
	global_load_dwordx4 v[178:181], v52, s[10:11] offset:3072
	s_sub_u32 s10, s10, 0x18000
	s_subb_u32 s11, s11, 0
	s_cmp_gt_i32 s2, 33
	s_cbranch_scc1 .LBB0_2216
	s_branch .LBB0_2194

; __device__ __forceinline__ int wg_row(int bid, int rl) { if (rl < 32) return (bid >> 7) * TB + CTXL + 32 * (bid & 127) + rl; const int q = 2 * bid + (rl - 32); return (q >> 8) * TB + (q & 255); }
; template <bool ROUTER, bool SMALLP>
; __device__ __forceinline__ void norm_phase(KA A, LAS unsigned char* lds, int l, int which, int npart, const float* pgate, int tid, int wave, int lane, int bid) {
;     ...
;     for (int rl = wave; rl < 34; rl += NWAVES) {
;         const int row = wg_row(bid, rl), s = row % TB; const bool isctx = s < CTXL; const int b = row / TB;
;         f32x4 v[8]; float ss = 0.f;
;         if (nb) {
; #pragma unroll
;             for (int jj = 0; jj < 4; ++jj) { float f[8]; unpack8(vnb[jj], f); v[2 * jj] = (f32x4){f[0], f[1], f[2], f[3]}; v[2 * jj + 1] = (f32x4){f[4], f[5], f[6], f[7]}; }
;         } else {
; #pragma unroll
;             for (int j = 0; j < 8; ++j) v[j] = vnx[j];
;         }
.LBB0_2200:
	s_cmp_lt_i32 s2, 32
	s_cselect_b32 vcc_lo, s101, 0
	s_cmp_lg_u32 vcc_lo, 0
	s_cbranch_scc0 .Lnbk_otop_B
	s_waitcnt vmcnt(12)
	s_branch .Lnbk_unpack_B

; template <bool ROUTER, bool SMALLP>
; __device__ __forceinline__ void norm_phase(KA A, LAS unsigned char* lds, int l, int which, int npart, const float* pgate, int tid, int wave, int lane, int bid) {
;     ...
;         if (rl + NWAVES < 34) NORM_LOAD(rl + NWAVES);
.LBB0_2202:
	s_cmp_gt_i32 s2, 25
	s_cselect_b64 s[8:9], -1, 0
	s_and_b64 vcc, exec, s[8:9]
	s_cbranch_vccnz .LBB0_2212
	s_cmp_lt_i32 s2, 24
	s_cselect_b32 vcc_lo, s101, 0
	s_cmp_lg_u32 vcc_lo, 0
	s_cbranch_scc0 .Lnbk_omid_B
	s_waitcnt vmcnt(8)
	s_cmp_gt_i32 s2, 7
	s_cbranch_scc1 .Lnbk_b2_B
	v_mov_b64_e32 v[34:35], v[134:135]
	v_mov_b64_e32 v[36:37], v[136:137]
	v_mov_b64_e32 v[38:39], v[138:139]
	v_mov_b64_e32 v[40:41], v[140:141]
	v_mov_b64_e32 v[42:43], v[142:143]
	v_mov_b64_e32 v[44:45], v[144:145]
	v_mov_b64_e32 v[46:47], v[146:147]
	v_mov_b64_e32 v[48:49], v[148:149]
	s_branch .LBB0_2212
.Lnbk_b2_B:
	s_cmp_gt_i32 s2, 15
	s_cbranch_scc1 .Lnbk_b3_B
	v_mov_b64_e32 v[34:35], v[150:151]
	v_mov_b64_e32 v[36:37], v[152:153]
	v_mov_b64_e32 v[38:39], v[154:155]
	v_mov_b64_e32 v[40:41], v[156:157]
	v_mov_b64_e32 v[42:43], v[158:159]
	v_mov_b64_e32 v[44:45], v[160:161]
	v_mov_b64_e32 v[46:47], v[162:163]
	v_mov_b64_e32 v[48:49], v[164:165]
	s_branch .LBB0_2212

.Lnbk_omid_B:
	s_cmp_gt_i32 s2, 23
	s_mov_b64 s[4:5], -1
	s_cbranch_scc0 .LBB0_2205
	s_add_i32 s4, s12, s2
	s_sub_i32 s4, s4, 24
	s_lshr_b32 s5, s4, 8
	s_mulk_i32 s5, 0x1100
	s_and_b32 s4, s4, 0xff
	s_or_b32 s6, s5, s4
	s_mov_b64 s[4:5], 0
